# combo7 + phase 1 conversion-first / GEMM-first workgroup groups split by XCD (block index bit 2) instead of 8-block stripes (bit 3)
# baseline (speedup 1.0000x reference)
.LBB0_128:
	s_cmp_lt_i32 s48, 2
	s_cselect_b64 s[6:7], -1, 0
	s_and_b64 s[12:13], s[6:7], s[4:5]
	s_andn2_b64 vcc, exec, s[12:13]
	s_cbranch_vccnz .LBB0_378
	s_bitcmp1_b32 s2, 2
	s_cselect_b64 s[10:11], -1, 0
	s_load_dwordx2 s[8:9], s[0:1], 0xb0
	s_cmpk_lt_i32 s2, 0x980
	s_cselect_b64 s[4:5], -1, 0
	s_and_b64 s[6:7], s[4:5], s[10:11]
	v_cndmask_b32_e64 v1, 0, 1, s[6:7]
	v_cmp_ne_u32_e64 s[4:5], 1, v1
	s_andn2_b64 vcc, exec, s[6:7]
	v_readfirstlane_b32 s20, v0
	s_cbranch_vccnz .LBB0_131
	s_ashr_i32 s6, s2, 31
	s_lshr_b32 s6, s6, 29
	s_add_i32 s6, s2, s6
	s_and_b32 s7, s6, -8
	s_sub_i32 s7, s2, s7
	s_cmp_lt_i32 s7, 0
	s_movk_i32 s14, 0x131
	s_cselect_b32 s14, s14, 0x130
	s_mul_i32 s7, s7, s14
	s_ashr_i32 s6, s6, 3
	s_add_i32 s7, s7, s6
	s_mul_hi_i32 s6, s7, 0x6bca1af3
	s_lshr_b32 s14, s6, 31
	s_ashr_i32 s6, s6, 7
	s_add_i32 s6, s6, s14
	s_lshl_b32 s14, s6, 3
	s_mulk_i32 s6, 0x130
	s_sub_i32 s6, s7, s6
	s_bfe_u32 s7, s6, 0x3001c
	s_add_i32 s7, s6, s7
	s_and_b32 s15, s7, 0xfff8
	s_sub_i32 s6, s6, s15
	s_sext_i32_i16 s6, s6
	s_add_i32 s30, s14, s6
	s_sext_i32_i16 s6, s7
	s_ashr_i32 s6, s6, 3
